# restructure: mixer-phase weight-conversion blocks are converted per wave (wave-private slice of the LDS tile), removing the per-block workgroup barrier
# baseline (speedup 1.0000x reference)
.LBB0_986:
	v_lshl_or_b32 v67, s13, 6, v66
	s_ashr_i32 s13, s12, 31
	s_lshl_b64 s[12:13], s[12:13], 3
	s_add_u32 s12, s0, s12
	s_addc_u32 s13, s1, s13
	s_load_dwordx2 s[12:13], s[12:13], 0x0
	v_ashrrev_i32_e32 v69, 6, v67
	v_lshrrev_b32_e32 v135, 3, v66
	v_lshlrev_b32_e32 v135, 4, v135
	v_and_b32_e32 v68, 63, v66
	v_and_b32_e32 v134, 7, v66
	v_lshlrev_b32_e32 v134, 2, v134
	v_lshl_or_b32 v134, v69, 5, v134
	s_waitcnt lgkmcnt(0)
	s_add_u32 s12, s12, s26
	s_addc_u32 s13, s13, s27
	s_add_u32 s12, s12, s28
	s_addc_u32 s13, s13, s29
	s_and_b32 s26, s11, 0x380
	v_add_u32_e32 v0, s26, v135
	v_mad_i64_i32 v[2:3], s[28:29], s24, v0, 0
	v_lshl_add_u64 v[2:3], v[2:3], 2, s[8:9]
	s_lshl_b32 s70, s10, 2
	v_lshl_add_u64 v[2:3], v[2:3], 0, s[70:71]
	v_lshlrev_b32_e32 v0, 2, v134
	v_lshl_add_u64 v[6:7], v[2:3], 0, v[0:1]
	s_lshl_b32 s70, s24, 2
	v_lshl_add_u64 v[10:11], v[6:7], 0, s[70:71]
	v_lshl_add_u64 v[14:15], v[10:11], 0, s[70:71]
	v_lshl_add_u64 v[18:19], v[14:15], 0, s[70:71]
	v_lshl_add_u64 v[22:23], v[18:19], 0, s[70:71]
	v_lshl_add_u64 v[26:27], v[22:23], 0, s[70:71]
	v_lshl_add_u64 v[30:31], v[26:27], 0, s[70:71]
	v_lshl_add_u64 v[34:35], v[30:31], 0, s[70:71]
	v_lshl_add_u64 v[38:39], v[34:35], 0, s[70:71]
	v_lshl_add_u64 v[42:43], v[38:39], 0, s[70:71]
	v_lshl_add_u64 v[46:47], v[42:43], 0, s[70:71]
	v_lshl_add_u64 v[50:51], v[46:47], 0, s[70:71]
	v_lshl_add_u64 v[54:55], v[50:51], 0, s[70:71]
	v_lshl_add_u64 v[58:59], v[54:55], 0, s[70:71]
	v_lshl_add_u64 v[62:63], v[58:59], 0, s[70:71]
	global_load_dwordx4 v[2:5], v[6:7], off nt
	v_lshl_add_u32 v0, v68, 9, 0
	global_load_dwordx4 v[6:9], v[10:11], off nt
	v_bitop3_b32 v68, v69, v66, 7 bitop3:0x78
	global_load_dwordx4 v[10:13], v[14:15], off nt
	v_lshrrev_b32_e32 v69, 5, v67
	global_load_dwordx4 v[14:17], v[18:19], off nt
	v_xor_b32_e32 v69, v69, v66
	global_load_dwordx4 v[18:21], v[22:23], off nt
	v_lshlrev_b32_e32 v69, 4, v69
	global_load_dwordx4 v[22:25], v[26:27], off nt
	v_ashrrev_i32_e32 v140, 3, v67
	global_load_dwordx4 v[26:29], v[30:31], off nt
	v_add_u32_e32 v70, 0x200, v67
	global_load_dwordx4 v[30:33], v[34:35], off nt
	v_add_u32_e32 v71, 0x400, v67
	global_load_dwordx4 v[34:37], v[38:39], off nt
	v_add_u32_e32 v67, 0x600, v67
	global_load_dwordx4 v[38:41], v[42:43], off nt
	v_and_b32_e32 v69, 0x70, v69
	global_load_dwordx4 v[42:45], v[46:47], off nt
	v_lshlrev_b32_e32 v66, 4, v66
	global_load_dwordx4 v[46:49], v[50:51], off nt
	v_ashrrev_i32_e32 v141, 3, v70
	global_load_dwordx4 v[50:53], v[54:55], off nt
	v_ashrrev_i32_e32 v142, 3, v71
	global_load_dwordx4 v[54:57], v[58:59], off nt
	v_ashrrev_i32_e32 v143, 3, v67
	global_load_dwordx4 v[58:61], v[62:63], off nt
	v_lshl_add_u64 v[62:63], v[62:63], 0, s[70:71]
	global_load_dwordx4 v[62:65], v[62:63], off nt
	v_lshlrev_b32_e32 v68, 4, v68
	v_add_u32_e32 v69, 0, v69
	v_and_b32_e32 v136, 0x70, v66
	v_lshlrev_b32_e32 v66, 7, v140
	v_lshlrev_b32_e32 v70, 7, v141
	v_lshlrev_b32_e32 v71, 7, v142
	v_lshlrev_b32_e32 v67, 7, v143
	v_mov_b32_e32 v137, v1
	v_add_u32_e32 v144, v0, v68
	v_add_u32_e32 v145, v69, v66
	v_add_u32_e32 v146, v69, v70
	v_add_u32_e32 v147, v69, v71
	v_add_u32_e32 v148, v69, v67
	v_lshrrev_b32_e32 v0, 3, v140
	v_and_b32_e32 v66, 7, v140
	v_lshrrev_b32_e32 v67, 4, v136
	v_xor_b32_e32 v68, v66, v67
	v_lshlrev_b32_e32 v68, 4, v68
	v_lshl_add_u32 v144, v134, 7, v68
	v_lshl_add_u32 v140, v0, 5, v66
	v_add_u32_e32 v141, 8, v140
	v_add_u32_e32 v142, 16, v140
	v_add_u32_e32 v143, 24, v140
	v_lshrrev_b32_e32 v68, 2, v140
	v_and_b32_e32 v68, 7, v68
	v_xor_b32_e32 v68, v68, v67
	v_lshlrev_b32_e32 v68, 4, v68
	v_lshl_add_u32 v145, v140, 7, v68
	v_lshrrev_b32_e32 v68, 2, v141
	v_and_b32_e32 v68, 7, v68
	v_xor_b32_e32 v68, v68, v67
	v_lshlrev_b32_e32 v68, 4, v68
	v_lshl_add_u32 v146, v141, 7, v68
	v_lshrrev_b32_e32 v68, 2, v142
	v_and_b32_e32 v68, 7, v68
	v_xor_b32_e32 v68, v68, v67
	v_lshlrev_b32_e32 v68, 4, v68
	v_lshl_add_u32 v147, v142, 7, v68
	v_lshrrev_b32_e32 v68, 2, v143
	v_and_b32_e32 v68, 7, v68
	v_xor_b32_e32 v68, v68, v67
	v_lshlrev_b32_e32 v68, 4, v68
	v_lshl_add_u32 v148, v143, 7, v68
	s_mov_b32 s37, s68
	s_mov_b32 s40, s51
	s_mov_b32 s41, s87
	s_mov_b32 s70, s26
	s_mov_b32 s45, s36
	s_mov_b32 s24, s10
	s_mov_b64 s[28:29], s[12:13]
	s_mov_b32 s44, s43
	s_branch .LBB0_990

.Lcvm_a_ready:
	v_mul_f32_e32 v0, 0x42800000, v2
	v_mul_f32_e32 v131, 0x42800000, v6
	v_mov_b32_e32 v130, v1
	v_cvt_pk_fp8_f32 v130, v0, v131
	v_mul_f32_e32 v132, 0x42800000, v10
	v_mul_f32_e32 v133, 0x42800000, v14
	v_mul_f32_e32 v0, 0x42800000, v18
	v_cvt_pk_fp8_f32 v130, v132, v133 op_sel:[0,0,1]
	v_mul_f32_e32 v132, 0x42800000, v22
	v_mov_b32_e32 v131, v1
	v_cvt_pk_fp8_f32 v131, v0, v132
	v_mul_f32_e32 v133, 0x42800000, v26
	v_mul_f32_e32 v138, 0x42800000, v30
	v_mul_f32_e32 v0, 0x42800000, v34
	v_cvt_pk_fp8_f32 v131, v133, v138 op_sel:[0,0,1]
	v_mul_f32_e32 v133, 0x42800000, v38
	v_mov_b32_e32 v132, v1
	v_cvt_pk_fp8_f32 v132, v0, v133
	v_mul_f32_e32 v138, 0x42800000, v42
	v_mul_f32_e32 v139, 0x42800000, v46
	v_mul_f32_e32 v0, 0x42800000, v50
	v_cvt_pk_fp8_f32 v132, v138, v139 op_sel:[0,0,1]
	v_mul_f32_e32 v138, 0x42800000, v54
	v_mov_b32_e32 v133, v1
	v_cvt_pk_fp8_f32 v133, v0, v138
	v_mul_f32_e32 v139, 0x42800000, v58
	v_mul_f32_e32 v149, 0x42800000, v62
	v_mul_f32_e32 v0, 0x42800000, v3
	v_cvt_pk_fp8_f32 v133, v139, v149 op_sel:[0,0,1]
	v_mul_f32_e32 v138, 0x42800000, v31
	v_mul_f32_e32 v139, 0x42800000, v47
	v_mul_f32_e32 v149, 0x42800000, v63
	ds_write_b128 v144, v[130:133]
	v_mul_f32_e32 v131, 0x42800000, v7
	v_mov_b32_e32 v130, v1
	v_cvt_pk_fp8_f32 v130, v0, v131
	v_mul_f32_e32 v132, 0x42800000, v11
	v_mul_f32_e32 v133, 0x42800000, v15
	v_mul_f32_e32 v0, 0x42800000, v19
	v_cvt_pk_fp8_f32 v130, v132, v133 op_sel:[0,0,1]
	v_mul_f32_e32 v132, 0x42800000, v23
	v_mov_b32_e32 v131, v1
	v_cvt_pk_fp8_f32 v131, v0, v132
	v_mul_f32_e32 v133, 0x42800000, v27
	v_mul_f32_e32 v0, 0x42800000, v35
	v_mov_b32_e32 v132, v1
	v_cvt_pk_fp8_f32 v131, v133, v138 op_sel:[0,0,1]
	v_mul_f32_e32 v133, 0x42800000, v39
	v_cvt_pk_fp8_f32 v132, v0, v133
	v_mul_f32_e32 v138, 0x42800000, v43
	v_mul_f32_e32 v0, 0x42800000, v51
	v_mov_b32_e32 v133, v1
	v_cvt_pk_fp8_f32 v132, v138, v139 op_sel:[0,0,1]
	v_mul_f32_e32 v138, 0x42800000, v55
	v_cvt_pk_fp8_f32 v133, v0, v138
	v_mul_f32_e32 v139, 0x42800000, v59
	v_mul_f32_e32 v0, 0x42800000, v4
	v_mul_f32_e32 v138, 0x42800000, v32
	v_cvt_pk_fp8_f32 v133, v139, v149 op_sel:[0,0,1]
	v_mul_f32_e32 v139, 0x42800000, v48
	v_mul_f32_e32 v149, 0x42800000, v64
	s_cmp_lg_u32 s36, 0
	ds_write_b128 v144, v[130:133] offset:128
	v_mul_f32_e32 v131, 0x42800000, v8
	v_mov_b32_e32 v130, v1
	v_cvt_pk_fp8_f32 v130, v0, v131
	v_mul_f32_e32 v132, 0x42800000, v12
	v_mul_f32_e32 v133, 0x42800000, v16
	v_mul_f32_e32 v0, 0x42800000, v20
	v_cvt_pk_fp8_f32 v130, v132, v133 op_sel:[0,0,1]
	v_mul_f32_e32 v132, 0x42800000, v24
	v_mov_b32_e32 v131, v1
	v_cvt_pk_fp8_f32 v131, v0, v132
	v_mul_f32_e32 v133, 0x42800000, v28
	v_mul_f32_e32 v0, 0x42800000, v36
	v_mov_b32_e32 v132, v1
	v_cvt_pk_fp8_f32 v131, v133, v138 op_sel:[0,0,1]
	v_mul_f32_e32 v133, 0x42800000, v40
	v_cvt_pk_fp8_f32 v132, v0, v133
	v_mul_f32_e32 v138, 0x42800000, v44
	v_mul_f32_e32 v0, 0x42800000, v52
	v_mov_b32_e32 v133, v1
	v_cvt_pk_fp8_f32 v132, v138, v139 op_sel:[0,0,1]
	v_mul_f32_e32 v138, 0x42800000, v56
	v_cvt_pk_fp8_f32 v133, v0, v138
	v_mul_f32_e32 v139, 0x42800000, v60
	v_mul_f32_e32 v0, 0x42800000, v5
	v_mul_f32_e32 v138, 0x42800000, v33
	v_cvt_pk_fp8_f32 v133, v139, v149 op_sel:[0,0,1]
	v_mul_f32_e32 v139, 0x42800000, v49
	v_mul_f32_e32 v149, 0x42800000, v65
	s_cselect_b64 s[34:35], -1, 0
	ds_write_b128 v144, v[130:133] offset:256
	v_mul_f32_e32 v131, 0x42800000, v9
	v_mov_b32_e32 v130, v1
	v_cvt_pk_fp8_f32 v130, v0, v131
	v_mul_f32_e32 v132, 0x42800000, v13
	v_mul_f32_e32 v133, 0x42800000, v17
	v_mul_f32_e32 v0, 0x42800000, v21
	v_cvt_pk_fp8_f32 v130, v132, v133 op_sel:[0,0,1]
	v_mul_f32_e32 v132, 0x42800000, v25
	v_mov_b32_e32 v131, v1
	v_cvt_pk_fp8_f32 v131, v0, v132
	v_mul_f32_e32 v133, 0x42800000, v29
	v_mul_f32_e32 v0, 0x42800000, v37
	v_mov_b32_e32 v132, v1
	v_cvt_pk_fp8_f32 v131, v133, v138 op_sel:[0,0,1]
	v_mul_f32_e32 v133, 0x42800000, v41
	v_cvt_pk_fp8_f32 v132, v0, v133
	v_mul_f32_e32 v138, 0x42800000, v45
	v_mul_f32_e32 v0, 0x42800000, v53
	v_mov_b32_e32 v133, v1
	v_cvt_pk_fp8_f32 v132, v138, v139 op_sel:[0,0,1]
	v_mul_f32_e32 v138, 0x42800000, v57
	v_cvt_pk_fp8_f32 v133, v0, v138
	v_mul_f32_e32 v139, 0x42800000, v61
	v_add_u32_e32 v138, s10, v140
	s_cmp_eq_u32 s36, 0
	v_cvt_pk_fp8_f32 v133, v139, v149 op_sel:[0,0,1]
	ds_write_b128 v144, v[130:133] offset:384
	s_waitcnt lgkmcnt(0)
	ds_read_b128 v[130:133], v145
	s_cbranch_scc1 .LBB0_1003
	v_cmp_lt_i32_e32 vcc, s47, v138
	v_lshlrev_b32_e32 v0, 1, v138
	v_and_b32_e32 v139, 0x7f, v138
	s_and_saveexec_b64 s[8:9], vcc
	s_xor_b64 s[8:9], exec, s[8:9]
	v_add_u32_e32 v0, 0x7ffff800, v0
	v_and_b32_e32 v0, 0x7fffff00, v0
	v_or3_b32 v138, v139, v0, s64
	s_andn2_saveexec_b64 s[8:9], s[8:9]
	v_and_or_b32 v138, v0, s65, v139
	s_or_b64 exec, exec, s[8:9]

.Lcvm_b_ready:
	v_mul_f32_e32 v0, 0x42800000, v70
	v_mul_f32_e32 v131, 0x42800000, v66
	v_mov_b32_e32 v130, v1
	v_cvt_pk_fp8_f32 v130, v0, v131
	v_mul_f32_e32 v132, 0x42800000, v78
	v_mul_f32_e32 v133, 0x42800000, v74
	v_mul_f32_e32 v0, 0x42800000, v86
	v_cvt_pk_fp8_f32 v130, v132, v133 op_sel:[0,0,1]
	v_mul_f32_e32 v132, 0x42800000, v82
	v_mov_b32_e32 v131, v1
	v_cvt_pk_fp8_f32 v131, v0, v132
	v_mul_f32_e32 v133, 0x42800000, v94
	v_mul_f32_e32 v138, 0x42800000, v90
	v_mul_f32_e32 v0, 0x42800000, v98
	v_cvt_pk_fp8_f32 v131, v133, v138 op_sel:[0,0,1]
	v_mul_f32_e32 v133, 0x42800000, v102
	v_mov_b32_e32 v132, v1
	v_cvt_pk_fp8_f32 v132, v0, v133
	v_mul_f32_e32 v138, 0x42800000, v106
	v_mul_f32_e32 v139, 0x42800000, v110
	v_mul_f32_e32 v0, 0x42800000, v114
	v_cvt_pk_fp8_f32 v132, v138, v139 op_sel:[0,0,1]
	v_mul_f32_e32 v138, 0x42800000, v118
	v_mov_b32_e32 v133, v1
	v_cvt_pk_fp8_f32 v133, v0, v138
	v_mul_f32_e32 v139, 0x42800000, v122
	v_mul_f32_e32 v149, 0x42800000, v126
	v_mul_f32_e32 v0, 0x42800000, v71
	v_cvt_pk_fp8_f32 v133, v139, v149 op_sel:[0,0,1]
	v_mul_f32_e32 v138, 0x42800000, v91
	v_mul_f32_e32 v139, 0x42800000, v111
	v_mul_f32_e32 v149, 0x42800000, v127
	ds_write_b128 v144, v[130:133] offset:32768
	v_mul_f32_e32 v131, 0x42800000, v67
	v_mov_b32_e32 v130, v1
	v_cvt_pk_fp8_f32 v130, v0, v131
	v_mul_f32_e32 v132, 0x42800000, v79
	v_mul_f32_e32 v133, 0x42800000, v75
	v_mul_f32_e32 v0, 0x42800000, v87
	v_cvt_pk_fp8_f32 v130, v132, v133 op_sel:[0,0,1]
	v_mul_f32_e32 v132, 0x42800000, v83
	v_mov_b32_e32 v131, v1
	v_cvt_pk_fp8_f32 v131, v0, v132
	v_mul_f32_e32 v133, 0x42800000, v95
	v_mul_f32_e32 v0, 0x42800000, v99
	v_mov_b32_e32 v132, v1
	v_cvt_pk_fp8_f32 v131, v133, v138 op_sel:[0,0,1]
	v_mul_f32_e32 v133, 0x42800000, v103
	v_cvt_pk_fp8_f32 v132, v0, v133
	v_mul_f32_e32 v138, 0x42800000, v107
	v_mul_f32_e32 v0, 0x42800000, v115
	v_mov_b32_e32 v133, v1
	v_cvt_pk_fp8_f32 v132, v138, v139 op_sel:[0,0,1]
	v_mul_f32_e32 v138, 0x42800000, v119
	v_cvt_pk_fp8_f32 v133, v0, v138
	v_mul_f32_e32 v139, 0x42800000, v123
	v_mul_f32_e32 v0, 0x42800000, v72
	v_mul_f32_e32 v138, 0x42800000, v92
	v_cvt_pk_fp8_f32 v133, v139, v149 op_sel:[0,0,1]
	v_mul_f32_e32 v139, 0x42800000, v112
	v_mul_f32_e32 v149, 0x42800000, v128
	s_cmp_lg_u32 s45, 0
	ds_write_b128 v144, v[130:133] offset:32896
	v_mul_f32_e32 v131, 0x42800000, v68
	v_mov_b32_e32 v130, v1
	v_cvt_pk_fp8_f32 v130, v0, v131
	v_mul_f32_e32 v132, 0x42800000, v80
	v_mul_f32_e32 v133, 0x42800000, v76
	v_mul_f32_e32 v0, 0x42800000, v88
	v_cvt_pk_fp8_f32 v130, v132, v133 op_sel:[0,0,1]
	v_mul_f32_e32 v132, 0x42800000, v84
	v_mov_b32_e32 v131, v1
	v_cvt_pk_fp8_f32 v131, v0, v132
	v_mul_f32_e32 v133, 0x42800000, v96
	v_mul_f32_e32 v0, 0x42800000, v100
	v_mov_b32_e32 v132, v1
	v_cvt_pk_fp8_f32 v131, v133, v138 op_sel:[0,0,1]
	v_mul_f32_e32 v133, 0x42800000, v104
	v_cvt_pk_fp8_f32 v132, v0, v133
	v_mul_f32_e32 v138, 0x42800000, v108
	v_mul_f32_e32 v0, 0x42800000, v116
	v_mov_b32_e32 v133, v1
	v_cvt_pk_fp8_f32 v132, v138, v139 op_sel:[0,0,1]
	v_mul_f32_e32 v138, 0x42800000, v120
	v_cvt_pk_fp8_f32 v133, v0, v138
	v_mul_f32_e32 v139, 0x42800000, v124
	v_mul_f32_e32 v0, 0x42800000, v73
	v_mul_f32_e32 v138, 0x42800000, v93
	v_cvt_pk_fp8_f32 v133, v139, v149 op_sel:[0,0,1]
	v_mul_f32_e32 v139, 0x42800000, v113
	v_mul_f32_e32 v149, 0x42800000, v129
	s_cselect_b64 s[34:35], -1, 0
	ds_write_b128 v144, v[130:133] offset:33024
	v_mul_f32_e32 v131, 0x42800000, v69
	v_mov_b32_e32 v130, v1
	v_cvt_pk_fp8_f32 v130, v0, v131
	v_mul_f32_e32 v132, 0x42800000, v81
	v_mul_f32_e32 v133, 0x42800000, v77
	v_mul_f32_e32 v0, 0x42800000, v89
	v_cvt_pk_fp8_f32 v130, v132, v133 op_sel:[0,0,1]
	v_mul_f32_e32 v132, 0x42800000, v85
	v_mov_b32_e32 v131, v1
	v_cvt_pk_fp8_f32 v131, v0, v132
	v_mul_f32_e32 v133, 0x42800000, v97
	v_mul_f32_e32 v0, 0x42800000, v101
	v_mov_b32_e32 v132, v1
	v_cvt_pk_fp8_f32 v131, v133, v138 op_sel:[0,0,1]
	v_mul_f32_e32 v133, 0x42800000, v105
	v_cvt_pk_fp8_f32 v132, v0, v133
	v_mul_f32_e32 v138, 0x42800000, v109
	v_mul_f32_e32 v0, 0x42800000, v117
	v_mov_b32_e32 v133, v1
	v_cvt_pk_fp8_f32 v132, v138, v139 op_sel:[0,0,1]
	v_mul_f32_e32 v138, 0x42800000, v121
	v_cvt_pk_fp8_f32 v133, v0, v138
	v_mul_f32_e32 v139, 0x42800000, v125
	v_add_u32_e32 v138, s24, v140
	s_cmp_eq_u32 s45, 0
	v_cvt_pk_fp8_f32 v133, v139, v149 op_sel:[0,0,1]
	ds_write_b128 v144, v[130:133] offset:33152
	s_waitcnt lgkmcnt(0)
	ds_read_b128 v[130:133], v145 offset:32768
	s_cbranch_scc1 .LBB0_1035
	v_cmp_lt_i32_e32 vcc, s47, v138
	v_lshlrev_b32_e32 v0, 1, v138
	v_and_b32_e32 v139, 0x7f, v138
	s_and_saveexec_b64 s[8:9], vcc
	s_xor_b64 s[8:9], exec, s[8:9]
	v_add_u32_e32 v0, 0x7ffff800, v0
	v_and_b32_e32 v0, 0x7fffff00, v0
	v_or3_b32 v138, v139, v0, s64
	s_andn2_saveexec_b64 s[8:9], s[8:9]
	v_and_or_b32 v138, v0, s65, v139
	s_or_b64 exec, exec, s[8:9]
